# P10 pass-0 histogram: v_cmpx writes exec directly instead of v_cmp + s_and_saveexec/s_or (8 per tile)
# speedup vs baseline: 1.0030x; 1.0030x over previous
.LBB0_1125:
	s_waitcnt vmcnt(7)
	v_mfma_f32_32x32x16_f16 v[32:47], v[74:77], v[102:105], 0
	s_add_i32 s76, s24, 1
	s_lshl_b64 s[0:1], s[76:77], 13
	v_lshl_add_u64 v[48:49], v[148:149], 0, s[0:1]
	s_lshl_b32 s50, s24, 1
	s_mov_b32 s51, s77
	s_lshl_b64 s[0:1], s[50:51], 12
	s_waitcnt vmcnt(5)
	v_mfma_f32_32x32x16_f16 v[32:47], v[70:73], v[106:109], v[32:47]
	s_waitcnt vmcnt(3)
	v_mfma_f32_32x32x16_f16 v[32:47], v[66:69], v[110:113], v[32:47]
	v_mfma_f32_32x32x16_f16 v[16:31], v[82:85], v[102:105], 0
	s_waitcnt vmcnt(1)
	v_mfma_f32_32x32x16_f16 v[32:47], v[62:65], v[114:117], v[32:47]
	v_mfma_f32_32x32x16_f16 v[16:31], v[78:81], v[106:109], v[16:31]
	s_nop 10
	v_cvt_pkrtz_f16_f32 v0, v32, v33
	v_cvt_pkrtz_f16_f32 v1, v34, v35
	v_cvt_pkrtz_f16_f32 v2, v36, v37
	v_cvt_pkrtz_f16_f32 v3, v38, v39
	v_pk_max_f16 v0, v0, 0
	v_pk_max_f16 v1, v1, 0
	v_pk_max_f16 v2, v2, 0
	v_mfma_f32_32x32x16_f16 v[16:31], v[58:61], v[110:113], v[16:31]
	v_pk_max_f16 v3, v3, 0
	v_cvt_pkrtz_f16_f32 v32, v40, v41
	v_cvt_pkrtz_f16_f32 v33, v42, v43
	v_cvt_pkrtz_f16_f32 v34, v44, v45
	v_cvt_pkrtz_f16_f32 v35, v46, v47
	v_pk_max_f16 v32, v32, 0
	v_pk_max_f16 v33, v33, 0
	v_mfma_f32_32x32x16_f16 v[0:15], v[134:137], v[0:3], 0
	v_pk_max_f16 v34, v34, 0
	v_pk_max_f16 v35, v35, 0
	v_mfma_f32_32x32x16_f16 v[16:31], v[54:57], v[114:117], v[16:31]
	global_load_dwordx4 v[102:105], v[48:49], off offset:-4096
	global_load_dwordx4 v[106:109], v[48:49], off offset:-2048
	global_load_dwordx4 v[110:113], v[48:49], off
	global_load_dwordx4 v[114:117], v[48:49], off offset:2048
	v_mfma_f32_32x32x16_f16 v[0:15], v[130:133], v[32:35], v[0:15]
	s_nop 6
	v_cvt_pkrtz_f16_f32 v16, v16, v17
	v_cvt_pkrtz_f16_f32 v17, v18, v19
	v_cvt_pkrtz_f16_f32 v18, v20, v21
	v_cvt_pkrtz_f16_f32 v19, v22, v23
	v_pk_max_f16 v16, v16, 0
	v_pk_max_f16 v17, v17, 0
	v_pk_max_f16 v18, v18, 0
	v_pk_max_f16 v19, v19, 0
	s_nop 1
	v_mfma_f32_32x32x16_f16 v[0:15], v[126:129], v[16:19], v[0:15]
	v_cvt_pkrtz_f16_f32 v16, v24, v25
	v_cvt_pkrtz_f16_f32 v17, v26, v27
	v_cvt_pkrtz_f16_f32 v18, v28, v29
	v_cvt_pkrtz_f16_f32 v19, v30, v31
	v_pk_max_f16 v16, v16, 0
	v_pk_max_f16 v17, v17, 0
	v_pk_max_f16 v18, v18, 0
	v_pk_max_f16 v19, v19, 0
	v_mfma_f32_32x32x16_f16 v[20:35], v[74:77], v[118:121], 0
	s_nop 0
	v_mfma_f32_32x32x16_f16 v[0:15], v[122:125], v[16:19], v[0:15]
	v_mfma_f32_32x32x16_f16 v[4:19], v[82:85], v[118:121], 0
	s_nop 10
	v_cvt_pkrtz_f16_f32 v0, v0, v1
	v_cvt_pkrtz_f16_f32 v1, v2, v3
	v_lshl_add_u64 v[2:3], v[154:155], 0, s[0:1]
	v_mfma_f32_32x32x16_f16 v[20:35], v[70:73], v[98:101], v[20:35]
	v_mfma_f32_32x32x16_f16 v[4:19], v[78:81], v[98:101], v[4:19]
	v_mfma_f32_32x32x16_f16 v[20:35], v[66:69], v[94:97], v[20:35]
	v_mfma_f32_32x32x16_f16 v[4:19], v[58:61], v[94:97], v[4:19]
	s_waitcnt vmcnt(4)
	v_mfma_f32_32x32x16_f16 v[20:35], v[62:65], v[90:93], v[20:35]
	v_mfma_f32_32x32x16_f16 v[4:19], v[54:57], v[90:93], v[4:19]
	global_load_dwordx4 v[118:121], v[48:49], off offset:-3584
	global_load_dwordx4 v[98:101], v[48:49], off offset:-1536
	global_load_dwordx4 v[94:97], v[48:49], off offset:512
	global_load_dwordx4 v[90:93], v[48:49], off offset:2560
	s_nop 6
	v_cvt_pkrtz_f16_f32 v20, v20, v21
	v_cvt_pkrtz_f16_f32 v21, v22, v23
	v_cvt_pkrtz_f16_f32 v22, v24, v25
	v_cvt_pkrtz_f16_f32 v23, v26, v27
	v_pk_max_f16 v20, v20, 0
	v_pk_max_f16 v21, v21, 0
	v_pk_max_f16 v22, v22, 0
	v_pk_max_f16 v23, v23, 0
	v_cvt_pkrtz_f16_f32 v4, v4, v5
	v_cvt_pkrtz_f16_f32 v5, v6, v7
	v_mfma_f32_32x32x16_f16 v[36:51], v[134:137], v[20:23], 0
	v_cvt_pkrtz_f16_f32 v20, v28, v29
	v_cvt_pkrtz_f16_f32 v21, v30, v31
	v_cvt_pkrtz_f16_f32 v22, v32, v33
	v_cvt_pkrtz_f16_f32 v23, v34, v35
	v_pk_max_f16 v20, v20, 0
	v_pk_max_f16 v21, v21, 0
	v_pk_max_f16 v22, v22, 0
	v_pk_max_f16 v23, v23, 0
	v_cvt_pkrtz_f16_f32 v6, v8, v9
	v_cvt_pkrtz_f16_f32 v7, v10, v11
	v_mfma_f32_32x32x16_f16 v[36:51], v[130:133], v[20:23], v[36:51]
	v_pk_max_f16 v4, v4, 0
	v_pk_max_f16 v5, v5, 0
	v_pk_max_f16 v6, v6, 0
	v_pk_max_f16 v7, v7, 0
	global_store_dwordx2 v[2:3], v[0:1], off
	v_pk_fma_f16 v0, v0, v189, v190
	v_mfma_f32_32x32x16_f16 v[36:51], v[126:129], v[4:7], v[36:51]
	v_cvt_pkrtz_f16_f32 v4, v12, v13
	v_cvt_pkrtz_f16_f32 v5, v14, v15
	v_cvt_pkrtz_f16_f32 v6, v16, v17
	v_cvt_pkrtz_f16_f32 v7, v18, v19
	v_pk_max_f16 v4, v4, 0
	v_pk_max_f16 v5, v5, 0
	v_pk_max_f16 v6, v6, 0
	v_pk_max_f16 v7, v7, 0
	v_pk_max_f16 v0, v0, s44 op_sel_hi:[1,0]
	s_nop 0
	v_mfma_f32_32x32x16_f16 v[36:51], v[122:125], v[4:7], v[36:51]
	v_pk_min_f16 v0, v0, s45 op_sel_hi:[1,0]
	s_nop 0
	v_and_b32_e32 v2, 0x3ff, v0
	s_waitcnt lgkmcnt(0)
	v_cmpx_ge_i32_e32 vcc, v2, v86
	v_lshl_add_u32 v2, v2, 2, v168
	ds_add_u32 v2, v183 offset:24576
	s_mov_b64 exec, -1
	v_bfe_u32 v0, v0, 16, 10
	v_cmpx_ge_i32_e32 vcc, v0, v87
	v_lshl_add_u32 v0, v0, 2, v169
	ds_add_u32 v0, v183 offset:24576
	s_mov_b64 exec, -1
	v_pk_fma_f16 v0, v1, v52, v188
	s_nop 0
	v_pk_max_f16 v0, v0, s44 op_sel_hi:[1,0]
	s_nop 0
	v_pk_min_f16 v0, v0, s45 op_sel_hi:[1,0]
	s_nop 0
	v_and_b32_e32 v1, 0x3ff, v0
	v_cmpx_ge_i32_e32 vcc, v1, v88
	v_lshl_add_u32 v1, v1, 2, v170
	ds_add_u32 v1, v183 offset:24576
	s_mov_b64 exec, -1
	v_bfe_u32 v0, v0, 16, 10
	v_cmpx_ge_i32_e32 vcc, v0, v89
	v_lshl_add_u32 v0, v0, 2, v171
	ds_add_u32 v0, v183 offset:24576
	s_mov_b64 exec, -1
	s_or_b32 s0, s50, 1
	s_mov_b32 s1, s77
	s_lshl_b64 s[0:1], s[0:1], 12
	v_cvt_pkrtz_f16_f32 v0, v36, v37
	v_cvt_pkrtz_f16_f32 v1, v38, v39
	v_lshl_add_u64 v[2:3], v[154:155], 0, s[0:1]
	global_store_dwordx2 v[2:3], v[0:1], off
	v_pk_fma_f16 v0, v0, v189, v190
	s_nop 0
	v_pk_max_f16 v0, v0, s44 op_sel_hi:[1,0]
	s_nop 0
	v_pk_min_f16 v0, v0, s45 op_sel_hi:[1,0]
	s_nop 0
	v_and_b32_e32 v2, 0x3ff, v0
	v_cmpx_ge_i32_e32 vcc, v2, v86
	v_lshl_add_u32 v2, v2, 2, v168
	ds_add_u32 v2, v183 offset:24576
	s_mov_b64 exec, -1
	v_bfe_u32 v0, v0, 16, 10
	v_cmpx_ge_i32_e32 vcc, v0, v87
	v_lshl_add_u32 v0, v0, 2, v169
	ds_add_u32 v0, v183 offset:24576
	s_mov_b64 exec, -1
	v_pk_fma_f16 v0, v1, v52, v188
	s_nop 0
	v_pk_max_f16 v0, v0, s44 op_sel_hi:[1,0]
	s_nop 0
	v_pk_min_f16 v0, v0, s45 op_sel_hi:[1,0]
	s_nop 0
	v_and_b32_e32 v1, 0x3ff, v0
	v_cmpx_ge_i32_e32 vcc, v1, v88
	v_lshl_add_u32 v1, v1, 2, v170
	ds_add_u32 v1, v183 offset:24576
	s_mov_b64 exec, -1
	v_bfe_u32 v0, v0, 16, 10
	v_cmpx_ge_i32_e32 vcc, v0, v89
	v_lshl_add_u32 v0, v0, 2, v171
	ds_add_u32 v0, v183 offset:24576
	s_mov_b64 exec, -1
	s_cmp_eq_u32 s24, 31
	s_cselect_b64 s[0:1], -1, 0
	s_and_b64 s[0:1], s[0:1], s[52:53]
	s_andn2_b64 vcc, exec, s[0:1]
	s_cbranch_vccnz .LBB0_1171
	s_waitcnt lgkmcnt(0)
	s_mov_b32 s24, 0
	s_mov_b32 s25, s41
	s_branch .LBB0_1146
